# P15 epilogue: lane-row exchange + dwordx4 stores; NSA tile loop: K/V LDS fragment reads pipelined (counted lgkmcnt, one base register)
# speedup vs baseline: 1.0290x; 1.0290x over previous
.LBB0_2419:
	s_lshl_b32 s2, s2, 13
	s_add_i32 s76, s2, 0
	s_add_i32 s76, s76, 0x10000
	s_andn2_b64 vcc, exec, s[8:9]
	v_lshlrev_b32_e32 v134, 2, v162
	s_cbranch_vccnz .LBB0_2468
	v_or_b32_e32 v6, 32, v168
	v_cmp_gt_i32_e64 s[40:41], v6, v2
	v_cmp_lt_i32_e64 s[42:43], v6, v2
	v_or_b32_e32 v6, 34, v168
	v_cmp_gt_i32_e64 s[44:45], v6, v2
	v_or_b32_e32 v6, 35, v168
	v_cmp_gt_i32_e64 s[46:47], v6, v2
	v_or_b32_e32 v6, 40, v168
	v_cmp_gt_i32_e64 s[48:49], v6, v2
	v_or_b32_e32 v6, 41, v168
	v_cmp_gt_i32_e64 s[50:51], v6, v2
	v_or_b32_e32 v6, 42, v168
	v_cmp_gt_i32_e64 s[52:53], v6, v2
	v_or_b32_e32 v6, 43, v168
	v_cmp_gt_i32_e64 s[54:55], v6, v2
	v_or_b32_e32 v6, 48, v168
	v_cmp_gt_i32_e64 s[56:57], v6, v2
	v_or_b32_e32 v6, 49, v168
	v_cmp_gt_i32_e64 s[58:59], v6, v2
	v_or_b32_e32 v6, 50, v168
	v_cmp_gt_i32_e64 s[60:61], v6, v2
	v_or_b32_e32 v6, 51, v168
	v_cmp_gt_i32_e64 s[62:63], v6, v2
	v_or_b32_e32 v6, 56, v168
	v_cmp_gt_i32_e64 s[64:65], v6, v2
	v_or_b32_e32 v6, 57, v168
	v_cmp_gt_i32_e64 s[66:67], v6, v2
	v_or_b32_e32 v6, 58, v168
	v_cmp_gt_i32_e64 s[68:69], v6, v2
	v_or_b32_e32 v6, 59, v168
	v_cmp_gt_i32_e64 s[6:7], v168, v2
	v_cmp_lt_i32_e64 s[8:9], v168, v2
	v_cmp_gt_i32_e64 s[10:11], v135, v2
	v_cmp_gt_i32_e64 s[12:13], v169, v2
	v_cmp_gt_i32_e64 s[14:15], v170, v2
	v_cmp_gt_i32_e64 s[16:17], v171, v2
	v_cmp_gt_i32_e64 s[18:19], v172, v2
	v_cmp_gt_i32_e64 s[20:21], v173, v2
	v_cmp_gt_i32_e64 s[22:23], v174, v2
	v_cmp_gt_i32_e64 s[24:25], v175, v2
	v_cmp_gt_i32_e64 s[26:27], v176, v2
	v_cmp_gt_i32_e64 s[28:29], v177, v2
	v_cmp_gt_i32_e64 s[30:31], v178, v2
	v_cmp_gt_i32_e64 s[34:35], v179, v2
	v_cmp_gt_i32_e64 s[36:37], v180, v2
	v_cmp_gt_i32_e64 s[38:39], v181, v2
	v_cmp_gt_i32_e64 s[70:71], v6, v2
	s_min_u32 s2, s92, 8
	v_lshlrev_b32_e32 v2, 4, v4
	s_add_i32 s2, s92, s2
	v_and_b32_e32 v2, 0xc0, v2
	s_lshl_b32 s87, s2, 13
	v_lshl_or_b32 v2, v160, 8, v2
	v_readlane_b32 s2, v247, 4
	v_lshlrev_b32_e32 v5, 1, v4
	v_mov_b32_e32 v140, 0
	v_add_u32_e32 v185, s2, v2
	v_readlane_b32 s2, v247, 5
	s_movk_i32 s96, 0xc00
	s_add_i32 s91, s91, s92
	v_add_u32_e32 v187, s2, v2
	v_readlane_b32 s2, v247, 6
	s_add_i32 s93, s93, s3
	v_mov_b32_e32 v139, v131
	v_add_u32_e32 v188, s2, v2
	v_readlane_b32 s2, v247, 7
	s_mov_b32 s94, 2
	v_add_u32_e32 v183, s75, v134
	v_add_u32_e32 v189, s2, v2
	v_readlane_b32 s2, v247, 8
	v_add3_u32 v184, s76, v166, v134
	s_lshl_b32 s95, s92, 13
	v_add_u32_e32 v190, s2, v2
	v_readlane_b32 s2, v247, 9
	s_addk_i32 s87, 0x4000
	v_and_or_b32 v186, v5, 32, v3
	v_add_u32_e32 v191, s2, v2
	v_readlane_b32 s2, v247, 10
	s_add_i32 s86, s75, 0xc000
	s_mov_b32 s3, 0
	v_add_u32_e32 v192, s2, v2
	v_readlane_b32 s2, v247, 11
	v_mov_b32_e32 v202, 0
	v_mov_b32_e32 v3, v140
	v_add_u32_e32 v193, s2, v2
	v_readlane_b32 s2, v247, 12
	v_mov_b32_e32 v4, v140
	v_mov_b32_e32 v5, v140
	v_add_u32_e32 v194, s2, v2
	v_readlane_b32 s2, v247, 13
	v_mov_b32_e32 v6, v140
	v_mov_b32_e32 v7, v140
	v_add_u32_e32 v195, s2, v2
	v_readlane_b32 s2, v247, 14
	v_mov_b32_e32 v8, v140
	v_mov_b32_e32 v9, v140
	v_add_u32_e32 v196, s2, v2
	v_readlane_b32 s2, v247, 15
	v_mov_b32_e32 v10, v140
	v_mov_b32_e32 v11, v140
	v_add_u32_e32 v197, s2, v2
	v_readlane_b32 s2, v247, 16
	v_mov_b32_e32 v12, v140
	v_mov_b32_e32 v13, v140
	v_add_u32_e32 v198, s2, v2
	v_readlane_b32 s2, v247, 17
	v_mov_b32_e32 v14, v140
	v_mov_b32_e32 v15, v140
	v_add_u32_e32 v199, s2, v2
	v_readlane_b32 s2, v247, 21
	v_mov_b32_e32 v16, v140
	v_mov_b32_e32 v17, v140
	v_add_u32_e32 v200, s2, v2
	s_add_i32 s2, 0, 0x8000
	v_add_u32_e32 v201, s2, v2
	s_mov_b32 s2, 0
	v_mov_b32_e32 v2, 0
	v_mov_b32_e32 v18, 0
	v_mov_b32_e32 v19, v140
	v_mov_b32_e32 v20, v140
	v_mov_b32_e32 v21, v140
	v_mov_b32_e32 v22, v140
	v_mov_b32_e32 v23, v140
	v_add_u32_e32 v226, v201, v186
	v_mov_b32_e32 v24, v140
	v_mov_b32_e32 v25, v140
	v_mov_b32_e32 v26, v140
	v_mov_b32_e32 v27, v140
	v_mov_b32_e32 v28, v140
	v_mov_b32_e32 v29, v140
	v_mov_b32_e32 v30, v140
	v_mov_b32_e32 v31, v140
	v_mov_b32_e32 v32, v140
	v_mov_b32_e32 v33, v140
	s_branch .LBB0_2422

.LBB0_2422:
	s_mul_hi_u32 s97, s3, 0xaaaaaaab
	s_lshr_b32 s97, s97, 1
	s_mulk_i32 s97, 0xa000
	s_add_i32 s97, s97, s2
	v_add_u32_e32 v225, s97, v226
	s_add_i32 s80, s3, 2
	s_cmp_lt_u32 s80, s90
	s_cselect_b64 s[72:73], -1, 0
	s_cmp_ge_u32 s80, s90
	s_mov_b64 s[78:79], -1
	s_cbranch_scc0 .LBB0_2430
	s_cmp_ge_u32 s3, s91
	s_cbranch_scc0 .LBB0_2425
	s_waitcnt vmcnt(0) lgkmcnt(0)
	s_barrier
	s_mov_b64 s[78:79], 0

.LBB0_2436:
	v_cndmask_b32_e64 v50, 0, 1, s[78:79]
	v_cmp_ne_u32_e32 vcc, 0, v50
	s_cmp_lg_u64 vcc, 0
	s_cselect_b64 s[80:81], -1, 0
	s_and_b32 s82, s2, 0x6000
	v_add_u32_e32 v54, s82, v182
	ds_read_b128 v[228:231], v54 offset:512
	ds_read_b128 v[232:235], v54 offset:2560
	ds_read_b128 v[236:239], v54 offset:4608
	ds_read_b128 v[240:243], v54 offset:6656
	s_waitcnt lgkmcnt(3)
	v_mfma_f32_32x32x16_bf16 v[82:97], v[228:231], v[114:117], v[34:49]
	s_waitcnt lgkmcnt(2)
	v_mfma_f32_32x32x16_bf16 v[82:97], v[232:235], v[118:121], v[82:97]
	s_waitcnt lgkmcnt(1)
	v_mfma_f32_32x32x16_bf16 v[82:97], v[236:239], v[122:125], v[82:97]
	s_waitcnt lgkmcnt(0)
	v_mfma_f32_32x32x16_bf16 v[82:97], v[240:243], v[126:129], v[82:97]
	ds_read_b64_tr_b16 v[228:229], v225
	ds_read_b64_tr_b16 v[230:231], v225 offset:512
	ds_read_b64_tr_b16 v[232:233], v225 offset:1024
	ds_read_b64_tr_b16 v[234:235], v225 offset:1536
	ds_read_b64_tr_b16 v[236:237], v225 offset:4096
	ds_read_b64_tr_b16 v[238:239], v225 offset:4608
	ds_read_b64_tr_b16 v[240:241], v225 offset:5120
	ds_read_b64_tr_b16 v[242:243], v225 offset:5632
	s_cbranch_vccz .LBB0_2438
	v_cndmask_b32_e64 v98, v98, v1, s[78:79]
	v_cndmask_b32_e64 v99, v99, v1, s[78:79]
	v_cndmask_b32_e64 v100, v100, v1, s[78:79]
	v_cndmask_b32_e64 v101, v101, v1, s[78:79]
	v_cndmask_b32_e64 v102, v102, v1, s[78:79]
	v_cndmask_b32_e64 v103, v103, v1, s[78:79]
	v_cndmask_b32_e64 v104, v104, v1, s[78:79]
	v_cndmask_b32_e64 v105, v105, v1, s[78:79]
	v_cndmask_b32_e64 v106, v106, v1, s[78:79]
	v_cndmask_b32_e64 v107, v107, v1, s[78:79]
	v_cndmask_b32_e64 v108, v108, v1, s[78:79]
	v_cndmask_b32_e64 v109, v109, v1, s[78:79]
	v_cndmask_b32_e64 v110, v110, v1, s[78:79]
	v_cndmask_b32_e64 v111, v111, v1, s[78:79]
	v_cndmask_b32_e64 v112, v112, v1, s[78:79]
	v_cndmask_b32_e64 v113, v113, v1, s[78:79]

.LBB0_2449:
	v_exp_f32_e32 v142, v112
	v_exp_f32_e32 v143, v113
	v_exp_f32_e32 v144, v110
	v_exp_f32_e32 v145, v111
	v_exp_f32_e32 v146, v108
	v_exp_f32_e32 v147, v109
	v_exp_f32_e32 v148, v106
	v_exp_f32_e32 v149, v107
	v_exp_f32_e32 v150, v104
	v_exp_f32_e32 v151, v105
	v_exp_f32_e32 v152, v102
	v_exp_f32_e32 v153, v103
	v_exp_f32_e32 v154, v100
	v_exp_f32_e32 v155, v101
	v_exp_f32_e32 v156, v98
	v_exp_f32_e32 v157, v99
	v_cvt_pk_bf16_f32 v98, v142, v143
	v_cvt_pk_bf16_f32 v99, v144, v145
	v_cvt_pk_bf16_f32 v100, v146, v147
	v_cvt_pk_bf16_f32 v101, v148, v149
	v_cvt_pk_bf16_f32 v102, v150, v151
	v_cvt_pk_bf16_f32 v103, v152, v153
	v_cvt_pk_bf16_f32 v104, v154, v155
	v_cvt_pk_bf16_f32 v105, v156, v157
	s_add_i32 s3, s3, 1
	s_waitcnt lgkmcnt(0)
	v_mfma_f32_32x32x16_bf16 v[2:17], v[98:101], v[228:231], v[2:17]
	v_mfma_f32_32x32x16_bf16 v[2:17], v[102:105], v[232:235], v[2:17]
	v_mfma_f32_32x32x16_bf16 v[18:33], v[98:101], v[236:239], v[18:33]
	v_mfma_f32_32x32x16_bf16 v[18:33], v[102:105], v[240:243], v[18:33]
	s_cmp_ge_u32 s3, s90
	s_cbranch_scc1 .LBB0_2451
	s_add_i32 s85, s2, 0x2000
	s_and_b32 s85, s85, 0x6000
	v_add_u32_e32 v102, s85, v182
	ds_read_b128 v[228:231], v102
	ds_read_b128 v[232:235], v102 offset:2048
	ds_read_b128 v[236:239], v102 offset:4096
	ds_read_b128 v[240:243], v102 offset:6144
	s_waitcnt lgkmcnt(3)
	v_mfma_f32_32x32x16_bf16 v[50:65], v[228:231], v[114:117], v[34:49]
	s_waitcnt lgkmcnt(2)
	v_mfma_f32_32x32x16_bf16 v[50:65], v[232:235], v[118:121], v[50:65]
	s_waitcnt lgkmcnt(1)
	v_mfma_f32_32x32x16_bf16 v[50:65], v[236:239], v[122:125], v[50:65]
	s_waitcnt lgkmcnt(0)
	v_mfma_f32_32x32x16_bf16 v[50:65], v[240:243], v[126:129], v[50:65]
.LBB0_2451:
	ds_read_b64_tr_b16 v[228:229], v225 offset:2048
	ds_read_b64_tr_b16 v[230:231], v225 offset:2560
	ds_read_b64_tr_b16 v[232:233], v225 offset:3072
	ds_read_b64_tr_b16 v[234:235], v225 offset:3584
	ds_read_b64_tr_b16 v[236:237], v225 offset:6144
	ds_read_b64_tr_b16 v[238:239], v225 offset:6656
	ds_read_b64_tr_b16 v[240:241], v225 offset:7168
	ds_read_b64_tr_b16 v[242:243], v225 offset:7680
	s_andn2_b64 vcc, exec, s[80:81]
	s_cbranch_vccnz .LBB0_2453
	v_cndmask_b32_e64 v82, v82, v1, s[78:79]
	v_cndmask_b32_e64 v83, v83, v1, s[78:79]
	v_cndmask_b32_e64 v84, v84, v1, s[78:79]
	v_cndmask_b32_e64 v85, v85, v1, s[78:79]
	v_cndmask_b32_e64 v86, v86, v1, s[78:79]
	v_cndmask_b32_e64 v87, v87, v1, s[78:79]
	v_cndmask_b32_e64 v88, v88, v1, s[78:79]
	v_cndmask_b32_e64 v89, v89, v1, s[78:79]
	v_cndmask_b32_e64 v90, v90, v1, s[78:79]
	v_cndmask_b32_e64 v91, v91, v1, s[78:79]
	v_cndmask_b32_e64 v92, v92, v1, s[78:79]
	v_cndmask_b32_e64 v93, v93, v1, s[78:79]
	v_cndmask_b32_e64 v94, v94, v1, s[78:79]
	v_cndmask_b32_e64 v95, v95, v1, s[78:79]
	v_cndmask_b32_e64 v96, v96, v1, s[78:79]
	v_cndmask_b32_e64 v97, v97, v1, s[78:79]

.LBB0_2463:
	v_exp_f32_e32 v84, v98
	v_exp_f32_e32 v85, v99
	v_exp_f32_e32 v86, v100
	v_exp_f32_e32 v87, v101
	v_exp_f32_e32 v88, v102
	v_exp_f32_e32 v89, v103
	v_exp_f32_e32 v90, v104
	v_exp_f32_e32 v91, v105
	v_exp_f32_e32 v92, v106
	v_exp_f32_e32 v93, v107
	v_exp_f32_e32 v94, v108
	v_exp_f32_e32 v95, v109
	v_exp_f32_e32 v96, v110
	v_exp_f32_e32 v97, v111
	v_exp_f32_e32 v98, v112
	v_exp_f32_e32 v99, v113
	v_pk_add_f32 v[100:101], v[86:87], v[84:85]
	v_pk_add_f32 v[102:103], v[90:91], v[88:89]
	s_nop 0
	v_pk_add_f32 v[100:101], v[102:103], v[100:101]
	v_pk_add_f32 v[102:103], v[94:95], v[92:93]
	v_pk_add_f32 v[104:105], v[98:99], v[96:97]
	s_nop 0
	v_pk_add_f32 v[102:103], v[104:105], v[102:103]
	s_nop 0
	v_pk_add_f32 v[100:101], v[102:103], v[100:101]
	s_nop 0
	v_add_f32_e32 v83, v100, v101
	v_add_f32_e32 v202, v82, v83
	v_cvt_pk_bf16_f32 v82, v84, v85
	v_cvt_pk_bf16_f32 v83, v86, v87
	v_cvt_pk_bf16_f32 v85, v90, v91
	v_cvt_pk_bf16_f32 v86, v92, v93
	v_cvt_pk_bf16_f32 v84, v88, v89
	v_cvt_pk_bf16_f32 v87, v94, v95
	v_cvt_pk_bf16_f32 v88, v96, v97
	v_cvt_pk_bf16_f32 v89, v98, v99
	s_cmp_lg_u32 s95, s2
	s_waitcnt lgkmcnt(0)
	v_mfma_f32_32x32x16_bf16 v[2:17], v[82:85], v[228:231], v[2:17]
	v_mfma_f32_32x32x16_bf16 v[2:17], v[86:89], v[232:235], v[2:17]
	v_mfma_f32_32x32x16_bf16 v[18:33], v[82:85], v[236:239], v[18:33]
	v_mfma_f32_32x32x16_bf16 v[18:33], v[86:89], v[240:243], v[18:33]
	s_cbranch_scc1 .LBB0_2466
	v_mov_b32_e32 v34, v202
	s_nop 1
	v_permlane32_swap_b32_e32 v202, v34
	s_and_saveexec_b64 s[72:73], s[4:5]
	s_cbranch_execz .LBB0_2421
	ds_read_b32 v35, v183 offset:57600
	v_add_f32_e32 v34, v202, v34
	s_waitcnt lgkmcnt(0)
	v_div_scale_f32 v36, s[78:79], v34, v34, v35
	v_rcp_f32_e32 v37, v36
	v_div_scale_f32 v38, vcc, v35, v34, v35
	v_fma_f32 v39, -v36, v37, 1.0
	v_fmac_f32_e32 v37, v39, v37
	v_mul_f32_e32 v39, v38, v37
	v_fma_f32 v40, -v36, v39, v38
	v_fmac_f32_e32 v39, v40, v37
	v_fma_f32 v36, -v36, v39, v38
	v_div_fmas_f32 v36, v36, v37, v39
	v_div_fixup_f32 v35, v36, v34, v35
	v_cmp_lt_f32_e32 vcc, 0, v34
	s_nop 1
	v_cndmask_b32_e32 v34, 0, v35, vcc
	ds_write_b32 v183, v34 offset:57472
	s_branch .LBB0_2421

.LBB0_4279:
.LBB0_4295:
	s_nop 15
	s_nop 7
	v_and_b32_e32 v144, 1, v150
	v_lshlrev_b32_e32 v144, 4, v144
	v_add3_u32 v146, v144, v1, s60
	v_and_b32_e32 v144, 2, v150
	v_lshlrev_b32_e32 v144, 3, v144
	v_mov_b32_e32 v145, 0
	v_add_u32_e32 v148, s12, v146
	v_mov_b32_e32 v149, 0
	v_lshlrev_b64 v[148:149], 11, v[148:149]
	s_lshl_b32 s42, s54, 8
	s_mov_b32 s43, 0
	v_lshl_add_u64 v[148:149], s[16:17], 0, v[148:149]
	v_lshl_add_u64 v[148:149], v[148:149], 0, s[42:43]
	v_lshl_add_u64 v[148:149], v[148:149], 0, s[18:19]
	v_lshl_add_u64 v[148:149], v[148:149], 0, v[144:145]
	s_mov_b64 s[44:45], 0x10000
	s_mov_b64 s[46:47], 0x40000
	s_mov_b64 s[48:49], 0x50000
	v_mul_f32_e32 v130, 0x3d800000, v130
	v_mul_f32_e32 v131, 0x3d800000, v131
	v_mul_f32_e32 v132, 0x3d800000, v132
	v_mul_f32_e32 v133, 0x3d800000, v133
	v_mul_f32_e32 v122, 0x3d800000, v122
	v_mul_f32_e32 v123, 0x3d800000, v123
	v_mul_f32_e32 v124, 0x3d800000, v124
	v_mul_f32_e32 v125, 0x3d800000, v125
	v_mul_f32_e32 v126, 0x3d800000, v126
	v_mul_f32_e32 v127, 0x3d800000, v127
	v_mul_f32_e32 v128, 0x3d800000, v128
	v_mul_f32_e32 v129, 0x3d800000, v129
	v_mul_f32_e32 v118, 0x3d800000, v118
	v_mul_f32_e32 v119, 0x3d800000, v119
	v_mul_f32_e32 v120, 0x3d800000, v120
	v_mul_f32_e32 v121, 0x3d800000, v121
	v_mul_f32_e32 v114, 0x3d800000, v114
	v_mul_f32_e32 v115, 0x3d800000, v115
	v_mul_f32_e32 v116, 0x3d800000, v116
	v_mul_f32_e32 v117, 0x3d800000, v117
	v_mul_f32_e32 v106, 0x3d800000, v106
	v_mul_f32_e32 v107, 0x3d800000, v107
	v_mul_f32_e32 v108, 0x3d800000, v108
	v_mul_f32_e32 v109, 0x3d800000, v109
	v_mul_f32_e32 v110, 0x3d800000, v110
	v_mul_f32_e32 v111, 0x3d800000, v111
	v_mul_f32_e32 v112, 0x3d800000, v112
	v_mul_f32_e32 v113, 0x3d800000, v113
	v_mul_f32_e32 v102, 0x3d800000, v102
	v_mul_f32_e32 v103, 0x3d800000, v103
	v_mul_f32_e32 v104, 0x3d800000, v104
	v_mul_f32_e32 v105, 0x3d800000, v105
	v_med3_f32 v130, v130, s68, v169
	v_med3_f32 v131, v131, s68, v169
	v_med3_f32 v132, v132, s68, v169
	v_med3_f32 v133, v133, s68, v169
	v_med3_f32 v122, v122, s68, v169
	v_med3_f32 v123, v123, s68, v169
	v_med3_f32 v124, v124, s68, v169
	v_med3_f32 v125, v125, s68, v169
	v_med3_f32 v126, v126, s68, v169
	v_med3_f32 v127, v127, s68, v169
	v_med3_f32 v128, v128, s68, v169
	v_med3_f32 v129, v129, s68, v169
	v_med3_f32 v118, v118, s68, v169
	v_med3_f32 v119, v119, s68, v169
	v_med3_f32 v120, v120, s68, v169
	v_med3_f32 v121, v121, s68, v169
	v_med3_f32 v114, v114, s68, v169
	v_med3_f32 v115, v115, s68, v169
	v_med3_f32 v116, v116, s68, v169
	v_med3_f32 v117, v117, s68, v169
	v_med3_f32 v106, v106, s68, v169
	v_med3_f32 v107, v107, s68, v169
	v_med3_f32 v108, v108, s68, v169
	v_med3_f32 v109, v109, s68, v169
	v_med3_f32 v110, v110, s68, v169
	v_med3_f32 v111, v111, s68, v169
	v_med3_f32 v112, v112, s68, v169
	v_med3_f32 v113, v113, s68, v169
	v_med3_f32 v102, v102, s68, v169
	v_med3_f32 v103, v103, s68, v169
	v_med3_f32 v104, v104, s68, v169
	v_med3_f32 v105, v105, s68, v169
	v_cvt_pk_fp8_f32 v176, v130, v131
	v_cvt_pk_fp8_f32 v177, v122, v123
	v_cvt_pk_fp8_f32 v178, v114, v115
	v_cvt_pk_fp8_f32 v179, v106, v107
	v_cvt_pk_fp8_f32 v180, v126, v127
	v_cvt_pk_fp8_f32 v181, v118, v119
	v_cvt_pk_fp8_f32 v182, v110, v111
	v_cvt_pk_fp8_f32 v183, v102, v103
	v_cvt_pk_fp8_f32 v176, v132, v133 op_sel:[0,0,1]
	v_cvt_pk_fp8_f32 v177, v124, v125 op_sel:[0,0,1]
	v_cvt_pk_fp8_f32 v178, v116, v117 op_sel:[0,0,1]
	v_cvt_pk_fp8_f32 v179, v108, v109 op_sel:[0,0,1]
	v_cvt_pk_fp8_f32 v180, v128, v129 op_sel:[0,0,1]
	v_cvt_pk_fp8_f32 v181, v120, v121 op_sel:[0,0,1]
	v_cvt_pk_fp8_f32 v182, v112, v113 op_sel:[0,0,1]
	v_cvt_pk_fp8_f32 v183, v104, v105 op_sel:[0,0,1]
	s_nop 1
	v_permlane16_swap_b32_e32 v176, v178
	v_permlane16_swap_b32_e32 v177, v179
	v_permlane16_swap_b32_e32 v180, v182
	v_permlane16_swap_b32_e32 v181, v183
	v_cmp_gt_i32_e32 vcc, s56, v146
	s_and_saveexec_b64 s[40:41], vcc
	s_cbranch_execz .Lp15_epi_skip0
	global_store_dwordx4 v[148:149], v[176:179], off
	global_store_dwordx4 v[148:149], v[180:183], off offset:128
.Lp15_epi_skip0:
	s_or_b64 exec, exec, s[40:41]
	v_mul_f32_e32 v98, 0x3d800000, v98
	v_mul_f32_e32 v99, 0x3d800000, v99
	v_mul_f32_e32 v100, 0x3d800000, v100
	v_mul_f32_e32 v101, 0x3d800000, v101
	v_mul_f32_e32 v90, 0x3d800000, v90
	v_mul_f32_e32 v91, 0x3d800000, v91
	v_mul_f32_e32 v92, 0x3d800000, v92
	v_mul_f32_e32 v93, 0x3d800000, v93
	v_mul_f32_e32 v94, 0x3d800000, v94
	v_mul_f32_e32 v95, 0x3d800000, v95
	v_mul_f32_e32 v96, 0x3d800000, v96
	v_mul_f32_e32 v97, 0x3d800000, v97
	v_mul_f32_e32 v86, 0x3d800000, v86
	v_mul_f32_e32 v87, 0x3d800000, v87
	v_mul_f32_e32 v88, 0x3d800000, v88
	v_mul_f32_e32 v89, 0x3d800000, v89
	v_mul_f32_e32 v74, 0x3d800000, v74
	v_mul_f32_e32 v75, 0x3d800000, v75
	v_mul_f32_e32 v76, 0x3d800000, v76
	v_mul_f32_e32 v77, 0x3d800000, v77
	v_mul_f32_e32 v58, 0x3d800000, v58
	v_mul_f32_e32 v59, 0x3d800000, v59
	v_mul_f32_e32 v60, 0x3d800000, v60
	v_mul_f32_e32 v61, 0x3d800000, v61
	v_mul_f32_e32 v62, 0x3d800000, v62
	v_mul_f32_e32 v63, 0x3d800000, v63
	v_mul_f32_e32 v64, 0x3d800000, v64
	v_mul_f32_e32 v65, 0x3d800000, v65
	v_mul_f32_e32 v54, 0x3d800000, v54
	v_mul_f32_e32 v55, 0x3d800000, v55
	v_mul_f32_e32 v56, 0x3d800000, v56
	v_mul_f32_e32 v57, 0x3d800000, v57
	v_med3_f32 v98, v98, s68, v169
	v_med3_f32 v99, v99, s68, v169
	v_med3_f32 v100, v100, s68, v169
	v_med3_f32 v101, v101, s68, v169
	v_med3_f32 v90, v90, s68, v169
	v_med3_f32 v91, v91, s68, v169
	v_med3_f32 v92, v92, s68, v169
	v_med3_f32 v93, v93, s68, v169
	v_med3_f32 v94, v94, s68, v169
	v_med3_f32 v95, v95, s68, v169
	v_med3_f32 v96, v96, s68, v169
	v_med3_f32 v97, v97, s68, v169
	v_med3_f32 v86, v86, s68, v169
	v_med3_f32 v87, v87, s68, v169
	v_med3_f32 v88, v88, s68, v169
	v_med3_f32 v89, v89, s68, v169
	v_med3_f32 v74, v74, s68, v169
	v_med3_f32 v75, v75, s68, v169
	v_med3_f32 v76, v76, s68, v169
	v_med3_f32 v77, v77, s68, v169
	v_med3_f32 v58, v58, s68, v169
	v_med3_f32 v59, v59, s68, v169
	v_med3_f32 v60, v60, s68, v169
	v_med3_f32 v61, v61, s68, v169
	v_med3_f32 v62, v62, s68, v169
	v_med3_f32 v63, v63, s68, v169
	v_med3_f32 v64, v64, s68, v169
	v_med3_f32 v65, v65, s68, v169
	v_med3_f32 v54, v54, s68, v169
	v_med3_f32 v55, v55, s68, v169
	v_med3_f32 v56, v56, s68, v169
	v_med3_f32 v57, v57, s68, v169
	v_cvt_pk_fp8_f32 v184, v98, v99
	v_cvt_pk_fp8_f32 v185, v90, v91
	v_cvt_pk_fp8_f32 v186, v74, v75
	v_cvt_pk_fp8_f32 v187, v58, v59
	v_cvt_pk_fp8_f32 v188, v94, v95
	v_cvt_pk_fp8_f32 v189, v86, v87
	v_cvt_pk_fp8_f32 v190, v62, v63
	v_cvt_pk_fp8_f32 v191, v54, v55
	v_cvt_pk_fp8_f32 v184, v100, v101 op_sel:[0,0,1]
	v_cvt_pk_fp8_f32 v185, v92, v93 op_sel:[0,0,1]
	v_cvt_pk_fp8_f32 v186, v76, v77 op_sel:[0,0,1]
	v_cvt_pk_fp8_f32 v187, v60, v61 op_sel:[0,0,1]
	v_cvt_pk_fp8_f32 v188, v96, v97 op_sel:[0,0,1]
	v_cvt_pk_fp8_f32 v189, v88, v89 op_sel:[0,0,1]
	v_cvt_pk_fp8_f32 v190, v64, v65 op_sel:[0,0,1]
	v_cvt_pk_fp8_f32 v191, v56, v57 op_sel:[0,0,1]
	s_nop 1
	v_permlane16_swap_b32_e32 v184, v186
	v_permlane16_swap_b32_e32 v185, v187
	v_permlane16_swap_b32_e32 v188, v190
	v_permlane16_swap_b32_e32 v189, v191
	v_add_u32_e32 v147, 32, v146
	v_cmp_gt_i32_e32 vcc, s56, v147
	v_lshl_add_u64 v[172:173], v[148:149], 0, s[44:45]
	s_and_saveexec_b64 s[40:41], vcc
	s_cbranch_execz .Lp15_epi_skip1
	global_store_dwordx4 v[172:173], v[184:187], off
	global_store_dwordx4 v[172:173], v[188:191], off offset:128
.Lp15_epi_skip1:
	s_or_b64 exec, exec, s[40:41]
	v_mul_f32_e32 v82, 0x3d800000, v82
	v_mul_f32_e32 v83, 0x3d800000, v83
	v_mul_f32_e32 v84, 0x3d800000, v84
	v_mul_f32_e32 v85, 0x3d800000, v85
	v_mul_f32_e32 v70, 0x3d800000, v70
	v_mul_f32_e32 v71, 0x3d800000, v71
	v_mul_f32_e32 v72, 0x3d800000, v72
	v_mul_f32_e32 v73, 0x3d800000, v73
	v_mul_f32_e32 v78, 0x3d800000, v78
	v_mul_f32_e32 v79, 0x3d800000, v79
	v_mul_f32_e32 v80, 0x3d800000, v80
	v_mul_f32_e32 v81, 0x3d800000, v81
	v_mul_f32_e32 v66, 0x3d800000, v66
	v_mul_f32_e32 v67, 0x3d800000, v67
	v_mul_f32_e32 v68, 0x3d800000, v68
	v_mul_f32_e32 v69, 0x3d800000, v69
	v_mul_f32_e32 v50, 0x3d800000, v50
	v_mul_f32_e32 v51, 0x3d800000, v51
	v_mul_f32_e32 v52, 0x3d800000, v52
	v_mul_f32_e32 v53, 0x3d800000, v53
	v_mul_f32_e32 v42, 0x3d800000, v42
	v_mul_f32_e32 v43, 0x3d800000, v43
	v_mul_f32_e32 v44, 0x3d800000, v44
	v_mul_f32_e32 v45, 0x3d800000, v45
	v_mul_f32_e32 v46, 0x3d800000, v46
	v_mul_f32_e32 v47, 0x3d800000, v47
	v_mul_f32_e32 v48, 0x3d800000, v48
	v_mul_f32_e32 v49, 0x3d800000, v49
	v_mul_f32_e32 v38, 0x3d800000, v38
	v_mul_f32_e32 v39, 0x3d800000, v39
	v_mul_f32_e32 v40, 0x3d800000, v40
	v_mul_f32_e32 v41, 0x3d800000, v41
	v_med3_f32 v82, v82, s68, v169
	v_med3_f32 v83, v83, s68, v169
	v_med3_f32 v84, v84, s68, v169
	v_med3_f32 v85, v85, s68, v169
	v_med3_f32 v70, v70, s68, v169
	v_med3_f32 v71, v71, s68, v169
	v_med3_f32 v72, v72, s68, v169
	v_med3_f32 v73, v73, s68, v169
	v_med3_f32 v78, v78, s68, v169
	v_med3_f32 v79, v79, s68, v169
	v_med3_f32 v80, v80, s68, v169
	v_med3_f32 v81, v81, s68, v169
	v_med3_f32 v66, v66, s68, v169
	v_med3_f32 v67, v67, s68, v169
	v_med3_f32 v68, v68, s68, v169
	v_med3_f32 v69, v69, s68, v169
	v_med3_f32 v50, v50, s68, v169
	v_med3_f32 v51, v51, s68, v169
	v_med3_f32 v52, v52, s68, v169
	v_med3_f32 v53, v53, s68, v169
	v_med3_f32 v42, v42, s68, v169
	v_med3_f32 v43, v43, s68, v169
	v_med3_f32 v44, v44, s68, v169
	v_med3_f32 v45, v45, s68, v169
	v_med3_f32 v46, v46, s68, v169
	v_med3_f32 v47, v47, s68, v169
	v_med3_f32 v48, v48, s68, v169
	v_med3_f32 v49, v49, s68, v169
	v_med3_f32 v38, v38, s68, v169
	v_med3_f32 v39, v39, s68, v169
	v_med3_f32 v40, v40, s68, v169
	v_med3_f32 v41, v41, s68, v169
	v_cvt_pk_fp8_f32 v192, v82, v83
	v_cvt_pk_fp8_f32 v193, v70, v71
	v_cvt_pk_fp8_f32 v194, v50, v51
	v_cvt_pk_fp8_f32 v195, v42, v43
	v_cvt_pk_fp8_f32 v196, v78, v79
	v_cvt_pk_fp8_f32 v197, v66, v67
	v_cvt_pk_fp8_f32 v198, v46, v47
	v_cvt_pk_fp8_f32 v199, v38, v39
	v_cvt_pk_fp8_f32 v192, v84, v85 op_sel:[0,0,1]
	v_cvt_pk_fp8_f32 v193, v72, v73 op_sel:[0,0,1]
	v_cvt_pk_fp8_f32 v194, v52, v53 op_sel:[0,0,1]
	v_cvt_pk_fp8_f32 v195, v44, v45 op_sel:[0,0,1]
	v_cvt_pk_fp8_f32 v196, v80, v81 op_sel:[0,0,1]
	v_cvt_pk_fp8_f32 v197, v68, v69 op_sel:[0,0,1]
	v_cvt_pk_fp8_f32 v198, v48, v49 op_sel:[0,0,1]
	v_cvt_pk_fp8_f32 v199, v40, v41 op_sel:[0,0,1]
	s_nop 1
	v_permlane16_swap_b32_e32 v192, v194
	v_permlane16_swap_b32_e32 v193, v195
	v_permlane16_swap_b32_e32 v196, v198
	v_permlane16_swap_b32_e32 v197, v199
	v_add_u32_e32 v147, 128, v146
	v_cmp_gt_i32_e32 vcc, s56, v147
	v_lshl_add_u64 v[172:173], v[148:149], 0, s[46:47]
	s_and_saveexec_b64 s[40:41], vcc
	s_cbranch_execz .Lp15_epi_skip2
	global_store_dwordx4 v[172:173], v[192:195], off
	global_store_dwordx4 v[172:173], v[196:199], off offset:128
.Lp15_epi_skip2:
	s_or_b64 exec, exec, s[40:41]
	v_mul_f32_e32 v34, 0x3d800000, v34
	v_mul_f32_e32 v35, 0x3d800000, v35
	v_mul_f32_e32 v36, 0x3d800000, v36
	v_mul_f32_e32 v37, 0x3d800000, v37
	v_mul_f32_e32 v26, 0x3d800000, v26
	v_mul_f32_e32 v27, 0x3d800000, v27
	v_mul_f32_e32 v28, 0x3d800000, v28
	v_mul_f32_e32 v29, 0x3d800000, v29
	v_mul_f32_e32 v30, 0x3d800000, v30
	v_mul_f32_e32 v31, 0x3d800000, v31
	v_mul_f32_e32 v32, 0x3d800000, v32
	v_mul_f32_e32 v33, 0x3d800000, v33
	v_mul_f32_e32 v22, 0x3d800000, v22
	v_mul_f32_e32 v23, 0x3d800000, v23
	v_mul_f32_e32 v24, 0x3d800000, v24
	v_mul_f32_e32 v25, 0x3d800000, v25
	v_mul_f32_e32 v18, 0x3d800000, v18
	v_mul_f32_e32 v19, 0x3d800000, v19
	v_mul_f32_e32 v20, 0x3d800000, v20
	v_mul_f32_e32 v21, 0x3d800000, v21
	v_mul_f32_e32 v10, 0x3d800000, v10
	v_mul_f32_e32 v11, 0x3d800000, v11
	v_mul_f32_e32 v12, 0x3d800000, v12
	v_mul_f32_e32 v13, 0x3d800000, v13
	v_mul_f32_e32 v14, 0x3d800000, v14
	v_mul_f32_e32 v15, 0x3d800000, v15
	v_mul_f32_e32 v16, 0x3d800000, v16
	v_mul_f32_e32 v17, 0x3d800000, v17
	v_mul_f32_e32 v6, 0x3d800000, v6
	v_mul_f32_e32 v7, 0x3d800000, v7
	v_mul_f32_e32 v8, 0x3d800000, v8
	v_mul_f32_e32 v9, 0x3d800000, v9
	v_med3_f32 v34, v34, s68, v169
	v_med3_f32 v35, v35, s68, v169
	v_med3_f32 v36, v36, s68, v169
	v_med3_f32 v37, v37, s68, v169
	v_med3_f32 v26, v26, s68, v169
	v_med3_f32 v27, v27, s68, v169
	v_med3_f32 v28, v28, s68, v169
	v_med3_f32 v29, v29, s68, v169
	v_med3_f32 v30, v30, s68, v169
	v_med3_f32 v31, v31, s68, v169
	v_med3_f32 v32, v32, s68, v169
	v_med3_f32 v33, v33, s68, v169
	v_med3_f32 v22, v22, s68, v169
	v_med3_f32 v23, v23, s68, v169
	v_med3_f32 v24, v24, s68, v169
	v_med3_f32 v25, v25, s68, v169
	v_med3_f32 v18, v18, s68, v169
	v_med3_f32 v19, v19, s68, v169
	v_med3_f32 v20, v20, s68, v169
	v_med3_f32 v21, v21, s68, v169
	v_med3_f32 v10, v10, s68, v169
	v_med3_f32 v11, v11, s68, v169
	v_med3_f32 v12, v12, s68, v169
	v_med3_f32 v13, v13, s68, v169
	v_med3_f32 v14, v14, s68, v169
	v_med3_f32 v15, v15, s68, v169
	v_med3_f32 v16, v16, s68, v169
	v_med3_f32 v17, v17, s68, v169
	v_med3_f32 v6, v6, s68, v169
	v_med3_f32 v7, v7, s68, v169
	v_med3_f32 v8, v8, s68, v169
	v_med3_f32 v9, v9, s68, v169
	v_cvt_pk_fp8_f32 v200, v34, v35
	v_cvt_pk_fp8_f32 v201, v26, v27
	v_cvt_pk_fp8_f32 v202, v18, v19
	v_cvt_pk_fp8_f32 v203, v10, v11
	v_cvt_pk_fp8_f32 v204, v30, v31
	v_cvt_pk_fp8_f32 v205, v22, v23
	v_cvt_pk_fp8_f32 v206, v14, v15
	v_cvt_pk_fp8_f32 v207, v6, v7
	v_cvt_pk_fp8_f32 v200, v36, v37 op_sel:[0,0,1]
	v_cvt_pk_fp8_f32 v201, v28, v29 op_sel:[0,0,1]
	v_cvt_pk_fp8_f32 v202, v20, v21 op_sel:[0,0,1]
	v_cvt_pk_fp8_f32 v203, v12, v13 op_sel:[0,0,1]
	v_cvt_pk_fp8_f32 v204, v32, v33 op_sel:[0,0,1]
	v_cvt_pk_fp8_f32 v205, v24, v25 op_sel:[0,0,1]
	v_cvt_pk_fp8_f32 v206, v16, v17 op_sel:[0,0,1]
	v_cvt_pk_fp8_f32 v207, v8, v9 op_sel:[0,0,1]
	s_nop 1
	v_permlane16_swap_b32_e32 v200, v202
	v_permlane16_swap_b32_e32 v201, v203
	v_permlane16_swap_b32_e32 v204, v206
	v_permlane16_swap_b32_e32 v205, v207
	v_add_u32_e32 v147, 160, v146
	v_cmp_gt_i32_e32 vcc, s56, v147
	v_lshl_add_u64 v[172:173], v[148:149], 0, s[48:49]
	s_and_saveexec_b64 s[40:41], vcc
	s_cbranch_execz .Lp15_epi_skip3
	global_store_dwordx4 v[172:173], v[200:203], off
	global_store_dwordx4 v[172:173], v[204:207], off offset:128
